# v31 + non-temporal hint on the read-once residual rows of the wout epilogue and the PP rows of the PLE-gate epilogue
# speedup vs baseline: 1.0691x; 1.0005x over previous
.LBB0_1858:
	s_lshl_b32 s13, s54, 8
	v_mbcnt_lo_u32_b32 v0, -1, 0
	v_mbcnt_hi_u32_b32 v0, -1, v0
	s_add_i32 s13, s13, s48
	v_and_or_b32 v4, v0, 15, s13
	s_lshl_b32 s13, s53, 8
	v_ashrrev_i32_e32 v0, 1, v0
	s_or_b32 s13, s13, s49
	v_and_b32_e32 v0, -8, v0
	v_add_u32_e32 v2, s13, v0
	v_ashrrev_i32_e32 v5, 31, v4
	v_ashrrev_i32_e32 v3, 31, v2
	v_lshlrev_b64 v[0:1], 10, v[4:5]
	v_lshl_add_u64 v[0:1], v[0:1], 0, v[2:3]
	v_lshlrev_b64 v[0:1], 1, v[0:1]
	v_lshl_add_u64 v[10:11], s[6:7], 0, v[0:1]
	global_load_dwordx4 v[6:9], v[10:11], off nt
	v_lshl_add_u64 v[16:17], s[8:9], 0, v[0:1]
	s_mov_b64 s[20:21], 0x40000
	s_andn2_b64 vcc, exec, s[40:41]
	s_waitcnt vmcnt(0)
	v_lshlrev_b32_e32 v5, 16, v6
	v_and_b32_e32 v6, 0xffff0000, v6
	v_lshlrev_b32_e32 v12, 16, v7
	v_lshlrev_b32_e32 v13, 16, v8
	v_and_b32_e32 v8, 0xffff0000, v8
	v_and_b32_e32 v7, 0xffff0000, v7
	v_lshlrev_b32_e32 v14, 16, v9
	v_and_b32_e32 v9, 0xffff0000, v9
	v_fmamk_f32 v6, v6, 0x3fd744fd, v159
	v_fmamk_f32 v12, v12, 0x3fd744fd, v160
	v_fmamk_f32 v13, v13, 0x3fd744fd, v154
	v_fmamk_f32 v8, v8, 0x3fd744fd, v155
	v_fmamk_f32 v5, v5, 0x3fd744fd, v158
	v_fmac_f32_e32 v161, 0x3fd744fd, v7
	v_fmamk_f32 v14, v14, 0x3fd744fd, v156
	v_fmac_f32_e32 v157, 0x3fd744fd, v9
	v_cvt_pk_bf16_f32 v6, v5, v6
	v_cvt_pk_bf16_f32 v7, v12, v161
	v_cvt_pk_bf16_f32 v8, v13, v8
	v_cvt_pk_bf16_f32 v9, v14, v157
	global_load_dwordx4 v[10:13], v[10:11], off offset:256 nt
	v_or_b32_e32 v14, 16, v4
	v_ashrrev_i32_e32 v15, 31, v14
	v_lshlrev_b64 v[14:15], 10, v[14:15]
	v_lshl_add_u64 v[14:15], v[14:15], 0, v[2:3]
	global_store_dwordx4 v[16:17], v[6:9], off
	v_lshlrev_b64 v[14:15], 1, v[14:15]
	v_lshl_add_u64 v[18:19], s[6:7], 0, v[14:15]
	v_lshl_add_u64 v[14:15], s[8:9], 0, v[14:15]
	s_waitcnt vmcnt(1)
	v_lshlrev_b32_e32 v5, 16, v10
	v_and_b32_e32 v6, 0xffff0000, v10
	v_lshlrev_b32_e32 v7, 16, v11
	v_and_b32_e32 v8, 0xffff0000, v11
	v_lshlrev_b32_e32 v9, 16, v12
	v_and_b32_e32 v10, 0xffff0000, v12
	v_lshlrev_b32_e32 v11, 16, v13
	v_and_b32_e32 v12, 0xffff0000, v13
	v_fmamk_f32 v6, v6, 0x3fd744fd, v151
	v_fmamk_f32 v7, v7, 0x3fd744fd, v152
	v_fmac_f32_e32 v153, 0x3fd744fd, v8
	v_fmamk_f32 v8, v9, 0x3fd744fd, v146
	v_fmamk_f32 v9, v10, 0x3fd744fd, v147
	v_fmamk_f32 v5, v5, 0x3fd744fd, v150
	v_fmamk_f32 v10, v11, 0x3fd744fd, v148
	v_fmac_f32_e32 v149, 0x3fd744fd, v12
	v_cvt_pk_bf16_f32 v6, v5, v6
	v_cvt_pk_bf16_f32 v7, v7, v153
	v_cvt_pk_bf16_f32 v8, v8, v9
	v_cvt_pk_bf16_f32 v9, v10, v149
	global_store_dwordx4 v[16:17], v[6:9], off offset:256
	global_load_dwordx4 v[6:9], v[18:19], off nt
	v_or_b32_e32 v16, 32, v4
	v_ashrrev_i32_e32 v17, 31, v16
	v_lshlrev_b64 v[16:17], 10, v[16:17]
	v_lshl_add_u64 v[16:17], v[16:17], 0, v[2:3]
	v_lshlrev_b64 v[16:17], 1, v[16:17]
	v_or_b32_e32 v4, 48, v4
	s_waitcnt vmcnt(0)
	v_lshlrev_b32_e32 v5, 16, v6
	v_and_b32_e32 v6, 0xffff0000, v6
	v_lshlrev_b32_e32 v10, 16, v7
	v_lshlrev_b32_e32 v11, 16, v8
	v_and_b32_e32 v8, 0xffff0000, v8
	v_lshlrev_b32_e32 v12, 16, v9
	v_and_b32_e32 v7, 0xffff0000, v7
	v_and_b32_e32 v9, 0xffff0000, v9
	v_fmamk_f32 v6, v6, 0x3fd744fd, v143
	v_fmamk_f32 v10, v10, 0x3fd744fd, v144
	v_fmamk_f32 v11, v11, 0x3fd744fd, v138
	v_fmamk_f32 v8, v8, 0x3fd744fd, v139
	v_fmamk_f32 v12, v12, 0x3fd744fd, v140
	v_fmamk_f32 v5, v5, 0x3fd744fd, v142
	v_fmac_f32_e32 v145, 0x3fd744fd, v7
	v_fmac_f32_e32 v141, 0x3fd744fd, v9
	v_cvt_pk_bf16_f32 v6, v5, v6
	v_cvt_pk_bf16_f32 v7, v10, v145
	v_cvt_pk_bf16_f32 v8, v11, v8
	v_cvt_pk_bf16_f32 v9, v12, v141
	global_load_dwordx4 v[10:13], v[18:19], off offset:256 nt
	v_lshl_add_u64 v[18:19], s[6:7], 0, v[16:17]
	global_store_dwordx4 v[14:15], v[6:9], off
	v_lshl_add_u64 v[16:17], s[8:9], 0, v[16:17]
	s_waitcnt vmcnt(1)
	v_lshlrev_b32_e32 v5, 16, v10
	v_and_b32_e32 v6, 0xffff0000, v10
	v_lshlrev_b32_e32 v7, 16, v11
	v_and_b32_e32 v8, 0xffff0000, v11
	v_lshlrev_b32_e32 v9, 16, v12
	v_and_b32_e32 v10, 0xffff0000, v12
	v_lshlrev_b32_e32 v11, 16, v13
	v_and_b32_e32 v12, 0xffff0000, v13
	v_fmamk_f32 v6, v6, 0x3fd744fd, v135
	v_fmamk_f32 v7, v7, 0x3fd744fd, v136
	v_fmac_f32_e32 v137, 0x3fd744fd, v8
	v_fmamk_f32 v8, v9, 0x3fd744fd, v130
	v_fmamk_f32 v9, v10, 0x3fd744fd, v131
	v_fmamk_f32 v5, v5, 0x3fd744fd, v134
	v_fmamk_f32 v10, v11, 0x3fd744fd, v132
	v_fmac_f32_e32 v133, 0x3fd744fd, v12
	v_cvt_pk_bf16_f32 v6, v5, v6
	v_cvt_pk_bf16_f32 v7, v7, v137
	v_cvt_pk_bf16_f32 v8, v8, v9
	v_cvt_pk_bf16_f32 v9, v10, v133
	global_store_dwordx4 v[14:15], v[6:9], off offset:256
	global_load_dwordx4 v[6:9], v[18:19], off nt
	s_waitcnt vmcnt(0)
	v_lshlrev_b32_e32 v5, 16, v6
	v_and_b32_e32 v6, 0xffff0000, v6
	v_lshlrev_b32_e32 v10, 16, v7
	v_lshlrev_b32_e32 v11, 16, v8
	v_and_b32_e32 v8, 0xffff0000, v8
	v_lshlrev_b32_e32 v12, 16, v9
	v_and_b32_e32 v7, 0xffff0000, v7
	v_and_b32_e32 v9, 0xffff0000, v9
	v_fmamk_f32 v6, v6, 0x3fd744fd, v127
	v_fmamk_f32 v10, v10, 0x3fd744fd, v128
	v_fmamk_f32 v11, v11, 0x3fd744fd, v122
	v_fmamk_f32 v8, v8, 0x3fd744fd, v123
	v_fmamk_f32 v12, v12, 0x3fd744fd, v124
	v_fmamk_f32 v5, v5, 0x3fd744fd, v126
	v_fmac_f32_e32 v129, 0x3fd744fd, v7
	v_fmac_f32_e32 v125, 0x3fd744fd, v9
	v_cvt_pk_bf16_f32 v6, v5, v6
	v_cvt_pk_bf16_f32 v7, v10, v129
	v_cvt_pk_bf16_f32 v8, v11, v8
	v_cvt_pk_bf16_f32 v9, v12, v125
	global_load_dwordx4 v[10:13], v[18:19], off offset:256 nt
	v_ashrrev_i32_e32 v5, 31, v4
	v_lshlrev_b64 v[4:5], 10, v[4:5]
	v_lshl_add_u64 v[2:3], v[4:5], 0, v[2:3]
	v_lshlrev_b64 v[14:15], 1, v[2:3]
	global_store_dwordx4 v[16:17], v[6:9], off
	v_lshl_add_u64 v[18:19], s[6:7], 0, v[14:15]
	s_waitcnt vmcnt(1)
	v_lshlrev_b32_e32 v2, 16, v10
	v_and_b32_e32 v3, 0xffff0000, v10
	v_lshlrev_b32_e32 v4, 16, v11
	v_and_b32_e32 v5, 0xffff0000, v11
	v_lshlrev_b32_e32 v6, 16, v12
	v_and_b32_e32 v7, 0xffff0000, v12
	v_lshlrev_b32_e32 v8, 16, v13
	v_and_b32_e32 v9, 0xffff0000, v13
	v_fmamk_f32 v2, v2, 0x3fd744fd, v118
	v_fmamk_f32 v3, v3, 0x3fd744fd, v119
	v_fmamk_f32 v4, v4, 0x3fd744fd, v120
	v_fmac_f32_e32 v121, 0x3fd744fd, v5
	v_fmamk_f32 v5, v6, 0x3fd744fd, v114
	v_fmamk_f32 v6, v7, 0x3fd744fd, v115
	v_fmamk_f32 v7, v8, 0x3fd744fd, v116
	v_fmac_f32_e32 v117, 0x3fd744fd, v9
	v_cvt_pk_bf16_f32 v2, v2, v3
	v_cvt_pk_bf16_f32 v3, v4, v121
	v_cvt_pk_bf16_f32 v4, v5, v6
	v_cvt_pk_bf16_f32 v5, v7, v117
	global_store_dwordx4 v[16:17], v[2:5], off offset:256
	global_load_dwordx4 v[2:5], v[18:19], off nt
	v_lshl_add_u64 v[12:13], s[8:9], 0, v[14:15]
	v_lshl_add_u64 v[10:11], v[0:1], 0, s[20:21]
	v_lshl_add_u64 v[14:15], s[6:7], 0, v[10:11]
	v_lshl_add_u64 v[10:11], s[8:9], 0, v[10:11]
	s_mov_b64 s[20:21], 0x48000
	s_waitcnt vmcnt(0)
	v_lshlrev_b32_e32 v6, 16, v2
	v_and_b32_e32 v2, 0xffff0000, v2
	v_lshlrev_b32_e32 v7, 16, v3
	v_lshlrev_b32_e32 v8, 16, v4
	v_and_b32_e32 v4, 0xffff0000, v4
	v_lshlrev_b32_e32 v9, 16, v5
	v_and_b32_e32 v3, 0xffff0000, v3
	v_and_b32_e32 v5, 0xffff0000, v5
	v_fmamk_f32 v6, v6, 0x3fd744fd, v110
	v_fmamk_f32 v2, v2, 0x3fd744fd, v111
	v_fmamk_f32 v7, v7, 0x3fd744fd, v112
	v_fmamk_f32 v8, v8, 0x3fd744fd, v106
	v_fmamk_f32 v4, v4, 0x3fd744fd, v107
	v_fmamk_f32 v9, v9, 0x3fd744fd, v108
	v_fmac_f32_e32 v113, 0x3fd744fd, v3
	v_fmac_f32_e32 v109, 0x3fd744fd, v5
	v_cvt_pk_bf16_f32 v2, v6, v2
	v_cvt_pk_bf16_f32 v3, v7, v113
	v_cvt_pk_bf16_f32 v4, v8, v4
	v_cvt_pk_bf16_f32 v5, v9, v109
	global_load_dwordx4 v[6:9], v[18:19], off offset:256 nt
	s_nop 0
	global_store_dwordx4 v[12:13], v[2:5], off
	s_waitcnt vmcnt(1)
	s_nop 0
	v_lshlrev_b32_e32 v2, 16, v6
	v_and_b32_e32 v3, 0xffff0000, v6
	v_lshlrev_b32_e32 v4, 16, v7
	v_and_b32_e32 v5, 0xffff0000, v7
	v_lshlrev_b32_e32 v6, 16, v8
	v_and_b32_e32 v7, 0xffff0000, v8
	v_lshlrev_b32_e32 v8, 16, v9
	v_and_b32_e32 v9, 0xffff0000, v9
	v_fmamk_f32 v2, v2, 0x3fd744fd, v102
	v_fmamk_f32 v3, v3, 0x3fd744fd, v103
	v_fmamk_f32 v4, v4, 0x3fd744fd, v104
	v_fmac_f32_e32 v105, 0x3fd744fd, v5
	v_fmamk_f32 v5, v6, 0x3fd744fd, v98
	v_fmamk_f32 v6, v7, 0x3fd744fd, v99
	v_fmamk_f32 v7, v8, 0x3fd744fd, v100
	v_fmac_f32_e32 v101, 0x3fd744fd, v9
	v_cvt_pk_bf16_f32 v2, v2, v3
	v_cvt_pk_bf16_f32 v3, v4, v105
	v_cvt_pk_bf16_f32 v4, v5, v6
	v_cvt_pk_bf16_f32 v5, v7, v101
	global_store_dwordx4 v[12:13], v[2:5], off offset:256
	global_load_dwordx4 v[2:5], v[14:15], off nt
	v_lshl_add_u64 v[12:13], v[0:1], 0, s[20:21]
	s_mov_b64 s[20:21], 0x50000
	s_waitcnt vmcnt(0)
	v_lshlrev_b32_e32 v6, 16, v2
	v_and_b32_e32 v2, 0xffff0000, v2
	v_lshlrev_b32_e32 v7, 16, v3
	v_lshlrev_b32_e32 v8, 16, v4
	v_and_b32_e32 v4, 0xffff0000, v4
	v_lshlrev_b32_e32 v9, 16, v5
	v_and_b32_e32 v3, 0xffff0000, v3
	v_and_b32_e32 v5, 0xffff0000, v5
	v_fmamk_f32 v6, v6, 0x3fd744fd, v94
	v_fmamk_f32 v2, v2, 0x3fd744fd, v95
	v_fmamk_f32 v7, v7, 0x3fd744fd, v96
	v_fmamk_f32 v8, v8, 0x3fd744fd, v90
	v_fmamk_f32 v4, v4, 0x3fd744fd, v91
	v_fmamk_f32 v9, v9, 0x3fd744fd, v92
	v_fmac_f32_e32 v97, 0x3fd744fd, v3
	v_fmac_f32_e32 v93, 0x3fd744fd, v5
	v_cvt_pk_bf16_f32 v2, v6, v2
	v_cvt_pk_bf16_f32 v3, v7, v97
	v_cvt_pk_bf16_f32 v4, v8, v4
	v_cvt_pk_bf16_f32 v5, v9, v93
	global_load_dwordx4 v[6:9], v[14:15], off offset:256 nt
	v_lshl_add_u64 v[14:15], s[6:7], 0, v[12:13]
	global_store_dwordx4 v[10:11], v[2:5], off
	v_lshl_add_u64 v[12:13], s[8:9], 0, v[12:13]
	s_waitcnt vmcnt(1)
	v_lshlrev_b32_e32 v2, 16, v6
	v_and_b32_e32 v3, 0xffff0000, v6
	v_lshlrev_b32_e32 v4, 16, v7
	v_and_b32_e32 v5, 0xffff0000, v7
	v_lshlrev_b32_e32 v6, 16, v8
	v_and_b32_e32 v7, 0xffff0000, v8
	v_lshlrev_b32_e32 v8, 16, v9
	v_and_b32_e32 v9, 0xffff0000, v9
	v_fmamk_f32 v2, v2, 0x3fd744fd, v86
	v_fmamk_f32 v3, v3, 0x3fd744fd, v87
	v_fmamk_f32 v4, v4, 0x3fd744fd, v88
	v_fmac_f32_e32 v89, 0x3fd744fd, v5
	v_fmamk_f32 v5, v6, 0x3fd744fd, v82
	v_fmamk_f32 v6, v7, 0x3fd744fd, v83
	v_fmamk_f32 v7, v8, 0x3fd744fd, v84
	v_fmac_f32_e32 v85, 0x3fd744fd, v9
	v_cvt_pk_bf16_f32 v2, v2, v3
	v_cvt_pk_bf16_f32 v3, v4, v89
	v_cvt_pk_bf16_f32 v4, v5, v6
	v_cvt_pk_bf16_f32 v5, v7, v85
	global_store_dwordx4 v[10:11], v[2:5], off offset:256
	global_load_dwordx4 v[2:5], v[14:15], off nt
	v_lshl_add_u64 v[10:11], v[0:1], 0, s[20:21]
	s_mov_b64 s[20:21], 0x58000
	s_waitcnt vmcnt(0)
	v_lshlrev_b32_e32 v6, 16, v2
	v_and_b32_e32 v2, 0xffff0000, v2
	v_lshlrev_b32_e32 v7, 16, v3
	v_lshlrev_b32_e32 v8, 16, v4
	v_and_b32_e32 v4, 0xffff0000, v4
	v_lshlrev_b32_e32 v9, 16, v5
	v_and_b32_e32 v3, 0xffff0000, v3
	v_and_b32_e32 v5, 0xffff0000, v5
	v_fmamk_f32 v6, v6, 0x3fd744fd, v78
	v_fmamk_f32 v2, v2, 0x3fd744fd, v79
	v_fmamk_f32 v7, v7, 0x3fd744fd, v80
	v_fmamk_f32 v8, v8, 0x3fd744fd, v74
	v_fmamk_f32 v4, v4, 0x3fd744fd, v75
	v_fmamk_f32 v9, v9, 0x3fd744fd, v76
	v_fmac_f32_e32 v81, 0x3fd744fd, v3
	v_fmac_f32_e32 v77, 0x3fd744fd, v5
	v_cvt_pk_bf16_f32 v2, v6, v2
	v_cvt_pk_bf16_f32 v3, v7, v81
	v_cvt_pk_bf16_f32 v4, v8, v4
	v_cvt_pk_bf16_f32 v5, v9, v77
	global_load_dwordx4 v[6:9], v[14:15], off offset:256 nt
	v_lshl_add_u64 v[14:15], s[6:7], 0, v[10:11]
	global_store_dwordx4 v[12:13], v[2:5], off
	v_lshl_add_u64 v[10:11], s[8:9], 0, v[10:11]
	s_waitcnt vmcnt(1)
	v_lshlrev_b32_e32 v2, 16, v6
	v_and_b32_e32 v3, 0xffff0000, v6
	v_lshlrev_b32_e32 v4, 16, v7
	v_and_b32_e32 v5, 0xffff0000, v7
	v_lshlrev_b32_e32 v6, 16, v8
	v_and_b32_e32 v7, 0xffff0000, v8
	v_lshlrev_b32_e32 v8, 16, v9
	v_and_b32_e32 v9, 0xffff0000, v9
	v_fmamk_f32 v2, v2, 0x3fd744fd, v70
	v_fmamk_f32 v3, v3, 0x3fd744fd, v71
	v_fmamk_f32 v4, v4, 0x3fd744fd, v72
	v_fmac_f32_e32 v73, 0x3fd744fd, v5
	v_fmamk_f32 v5, v6, 0x3fd744fd, v66
	v_fmamk_f32 v6, v7, 0x3fd744fd, v67
	v_fmamk_f32 v7, v8, 0x3fd744fd, v68
	v_fmac_f32_e32 v69, 0x3fd744fd, v9
	v_cvt_pk_bf16_f32 v2, v2, v3
	v_cvt_pk_bf16_f32 v3, v4, v73
	v_cvt_pk_bf16_f32 v4, v5, v6
	v_cvt_pk_bf16_f32 v5, v7, v69
	global_store_dwordx4 v[12:13], v[2:5], off offset:256
	global_load_dwordx4 v[2:5], v[14:15], off nt
	v_lshl_add_u64 v[12:13], v[0:1], 0, s[20:21]
	s_mov_b64 s[20:21], -1
	s_waitcnt vmcnt(0)
	v_lshlrev_b32_e32 v6, 16, v2
	v_and_b32_e32 v2, 0xffff0000, v2
	v_lshlrev_b32_e32 v7, 16, v3
	v_lshlrev_b32_e32 v8, 16, v4
	v_and_b32_e32 v4, 0xffff0000, v4
	v_lshlrev_b32_e32 v9, 16, v5
	v_and_b32_e32 v3, 0xffff0000, v3
	v_and_b32_e32 v5, 0xffff0000, v5
	v_fmamk_f32 v6, v6, 0x3fd744fd, v60
	v_fmamk_f32 v2, v2, 0x3fd744fd, v61
	v_fmamk_f32 v7, v7, 0x3fd744fd, v62
	v_fmamk_f32 v8, v8, 0x3fd744fd, v56
	v_fmamk_f32 v4, v4, 0x3fd744fd, v57
	v_fmamk_f32 v9, v9, 0x3fd744fd, v58
	v_fmac_f32_e32 v63, 0x3fd744fd, v3
	v_fmac_f32_e32 v59, 0x3fd744fd, v5
	v_cvt_pk_bf16_f32 v2, v6, v2
	v_cvt_pk_bf16_f32 v3, v7, v63
	v_cvt_pk_bf16_f32 v4, v8, v4
	v_cvt_pk_bf16_f32 v5, v9, v59
	global_load_dwordx4 v[6:9], v[14:15], off offset:256 nt
	v_lshl_add_u64 v[14:15], s[6:7], 0, v[12:13]
	global_store_dwordx4 v[10:11], v[2:5], off
	s_waitcnt vmcnt(1)
	v_lshlrev_b32_e32 v0, 16, v6
	v_and_b32_e32 v1, 0xffff0000, v6
	v_lshlrev_b32_e32 v2, 16, v7
	v_and_b32_e32 v3, 0xffff0000, v7
	v_lshlrev_b32_e32 v4, 16, v8
	v_and_b32_e32 v5, 0xffff0000, v8
	v_lshlrev_b32_e32 v6, 16, v9
	v_and_b32_e32 v7, 0xffff0000, v9
	v_fmamk_f32 v0, v0, 0x3fd744fd, v52
	v_fmamk_f32 v1, v1, 0x3fd744fd, v53
	v_fmamk_f32 v2, v2, 0x3fd744fd, v54
	v_fmac_f32_e32 v55, 0x3fd744fd, v3
	v_fmamk_f32 v3, v4, 0x3fd744fd, v48
	v_fmamk_f32 v4, v5, 0x3fd744fd, v49
	v_fmamk_f32 v5, v6, 0x3fd744fd, v50
	v_fmac_f32_e32 v51, 0x3fd744fd, v7
	v_cvt_pk_bf16_f32 v0, v0, v1
	v_cvt_pk_bf16_f32 v1, v2, v55
	v_cvt_pk_bf16_f32 v2, v3, v4
	v_cvt_pk_bf16_f32 v3, v5, v51
	global_store_dwordx4 v[10:11], v[0:3], off offset:256
	global_load_dwordx4 v[0:3], v[14:15], off nt
	v_lshl_add_u64 v[8:9], s[8:9], 0, v[12:13]
	s_waitcnt vmcnt(0)
	v_lshlrev_b32_e32 v4, 16, v0
	v_and_b32_e32 v0, 0xffff0000, v0
	v_lshlrev_b32_e32 v5, 16, v1
	v_lshlrev_b32_e32 v6, 16, v2
	v_and_b32_e32 v2, 0xffff0000, v2
	v_lshlrev_b32_e32 v7, 16, v3
	v_and_b32_e32 v1, 0xffff0000, v1
	v_and_b32_e32 v3, 0xffff0000, v3
	v_fmamk_f32 v4, v4, 0x3fd744fd, v44
	v_fmamk_f32 v0, v0, 0x3fd744fd, v45
	v_fmamk_f32 v5, v5, 0x3fd744fd, v46
	v_fmamk_f32 v6, v6, 0x3fd744fd, v40
	v_fmamk_f32 v2, v2, 0x3fd744fd, v41
	v_fmamk_f32 v7, v7, 0x3fd744fd, v42
	v_fmac_f32_e32 v47, 0x3fd744fd, v1
	v_fmac_f32_e32 v43, 0x3fd744fd, v3
	v_cvt_pk_bf16_f32 v0, v4, v0
	v_cvt_pk_bf16_f32 v1, v5, v47
	v_cvt_pk_bf16_f32 v2, v6, v2
	v_cvt_pk_bf16_f32 v3, v7, v43
	global_load_dwordx4 v[4:7], v[14:15], off offset:256 nt
	s_nop 0
	global_store_dwordx4 v[8:9], v[0:3], off
	s_waitcnt vmcnt(1)
	s_nop 0
	v_lshlrev_b32_e32 v0, 16, v4
	v_and_b32_e32 v1, 0xffff0000, v4
	v_lshlrev_b32_e32 v2, 16, v5
	v_and_b32_e32 v3, 0xffff0000, v5
	v_lshlrev_b32_e32 v4, 16, v6
	v_and_b32_e32 v5, 0xffff0000, v6
	v_lshlrev_b32_e32 v6, 16, v7
	v_and_b32_e32 v7, 0xffff0000, v7
	v_fmamk_f32 v0, v0, 0x3fd744fd, v36
	v_fmamk_f32 v1, v1, 0x3fd744fd, v37
	v_fmamk_f32 v2, v2, 0x3fd744fd, v38
	v_fmac_f32_e32 v39, 0x3fd744fd, v3
	v_fmamk_f32 v3, v4, 0x3fd744fd, v32
	v_fmamk_f32 v4, v5, 0x3fd744fd, v33
	v_fmamk_f32 v5, v6, 0x3fd744fd, v34
	v_fmac_f32_e32 v35, 0x3fd744fd, v7
	v_cvt_pk_bf16_f32 v0, v0, v1
	v_cvt_pk_bf16_f32 v1, v2, v39
	v_cvt_pk_bf16_f32 v2, v3, v4
	v_cvt_pk_bf16_f32 v3, v5, v35
	global_store_dwordx4 v[8:9], v[0:3], off offset:256
	s_cbranch_vccnz .LBB0_1847
	s_andn2_b64 vcc, exec, s[4:5]
	s_cbranch_vccnz .LBB0_1846
	s_barrier
	s_branch .LBB0_1846

.LBB0_2350:
	s_lshl_b32 s13, s52, 8
	v_mbcnt_lo_u32_b32 v0, -1, 0
	v_mbcnt_hi_u32_b32 v0, -1, v0
	s_add_i32 s13, s13, s46
	v_and_or_b32 v4, v0, 15, s13
	s_lshl_b32 s13, s51, 8
	v_ashrrev_i32_e32 v0, 1, v0
	s_or_b32 s13, s13, s47
	v_and_b32_e32 v0, -8, v0
	v_add_u32_e32 v2, s13, v0
	v_ashrrev_i32_e32 v5, 31, v4
	v_ashrrev_i32_e32 v3, 31, v2
	v_lshlrev_b64 v[0:1], 10, v[4:5]
	v_lshl_add_u64 v[0:1], v[0:1], 0, v[2:3]
	v_lshlrev_b64 v[0:1], 1, v[0:1]
	v_lshl_add_u64 v[10:11], s[6:7], 0, v[0:1]
	global_load_dwordx4 v[6:9], v[10:11], off nt
	v_mul_f32_e32 v12, 0xbfb8aa3b, v159
	v_mul_f32_e32 v13, 0xbfb8aa3b, v160
	v_mul_f32_e32 v14, 0xbfb8aa3b, v161
	v_mul_f32_e32 v15, 0xbfb8aa3b, v154
	v_mul_f32_e32 v16, 0xbfb8aa3b, v155
	v_mul_f32_e32 v18, 0xbfb8aa3b, v157
	v_mul_f32_e32 v5, 0xbfb8aa3b, v158
	v_mul_f32_e32 v17, 0xbfb8aa3b, v156
	v_exp_f32_e32 v12, v12
	v_exp_f32_e32 v13, v13
	v_exp_f32_e32 v14, v14
	v_exp_f32_e32 v15, v15
	v_exp_f32_e32 v16, v16
	v_exp_f32_e32 v18, v18
	v_exp_f32_e32 v5, v5
	v_exp_f32_e32 v17, v17
	v_add_f32_e32 v12, 1.0, v12
	v_add_f32_e32 v13, 1.0, v13
	v_add_f32_e32 v14, 1.0, v14
	v_add_f32_e32 v15, 1.0, v15
	v_add_f32_e32 v16, 1.0, v16
	v_add_f32_e32 v18, 1.0, v18
	v_add_f32_e32 v5, 1.0, v5
	v_add_f32_e32 v17, 1.0, v17
	v_rcp_f32_e32 v12, v12
	v_rcp_f32_e32 v13, v13
	v_rcp_f32_e32 v14, v14
	v_rcp_f32_e32 v15, v15
	v_rcp_f32_e32 v16, v16
	v_rcp_f32_e32 v18, v18
	v_rcp_f32_e32 v5, v5
	v_rcp_f32_e32 v17, v17
	s_mov_b64 s[20:21], 0x40000
	s_andn2_b64 vcc, exec, s[38:39]
	s_waitcnt vmcnt(0)
	v_lshlrev_b32_e32 v19, 16, v6
	v_and_b32_e32 v6, 0xffff0000, v6
	v_lshlrev_b32_e32 v20, 16, v7
	v_and_b32_e32 v7, 0xffff0000, v7
	v_lshlrev_b32_e32 v21, 16, v8
	v_and_b32_e32 v8, 0xffff0000, v8
	v_lshlrev_b32_e32 v22, 16, v9
	v_and_b32_e32 v9, 0xffff0000, v9
	v_mul_f32_e32 v6, v12, v6
	v_mul_f32_e32 v12, v13, v20
	v_mul_f32_e32 v7, v14, v7
	v_mul_f32_e32 v13, v15, v21
	v_mul_f32_e32 v8, v16, v8
	v_mul_f32_e32 v9, v18, v9
	v_mul_f32_e32 v5, v5, v19
	v_mul_f32_e32 v14, v17, v22
	v_cvt_pk_bf16_f32 v6, v5, v6
	v_cvt_pk_bf16_f32 v7, v12, v7
	v_cvt_pk_bf16_f32 v8, v13, v8
	v_cvt_pk_bf16_f32 v9, v14, v9
	global_load_dwordx4 v[10:13], v[10:11], off offset:256 nt
	v_mul_f32_e32 v5, 0xbfb8aa3b, v150
	v_mul_f32_e32 v14, 0xbfb8aa3b, v151
	v_mul_f32_e32 v15, 0xbfb8aa3b, v152
	v_mul_f32_e32 v16, 0xbfb8aa3b, v153
	v_mul_f32_e32 v17, 0xbfb8aa3b, v146
	v_mul_f32_e32 v18, 0xbfb8aa3b, v147
	v_mul_f32_e32 v19, 0xbfb8aa3b, v148
	v_mul_f32_e32 v20, 0xbfb8aa3b, v149
	v_exp_f32_e32 v5, v5
	v_exp_f32_e32 v21, v14
	v_exp_f32_e32 v22, v15
	v_exp_f32_e32 v16, v16
	v_exp_f32_e32 v17, v17
	v_exp_f32_e32 v18, v18
	v_exp_f32_e32 v19, v19
	v_exp_f32_e32 v20, v20
	v_add_f32_e32 v5, 1.0, v5
	v_add_f32_e32 v21, 1.0, v21
	v_add_f32_e32 v22, 1.0, v22
	v_add_f32_e32 v16, 1.0, v16
	v_add_f32_e32 v17, 1.0, v17
	v_or_b32_e32 v14, 16, v4
	v_add_f32_e32 v18, 1.0, v18
	v_add_f32_e32 v19, 1.0, v19
	v_add_f32_e32 v20, 1.0, v20
	v_rcp_f32_e32 v5, v5
	v_rcp_f32_e32 v21, v21
	v_rcp_f32_e32 v22, v22
	v_rcp_f32_e32 v23, v16
	v_rcp_f32_e32 v24, v17
	v_ashrrev_i32_e32 v15, 31, v14
	v_rcp_f32_e32 v25, v18
	v_rcp_f32_e32 v26, v19
	v_rcp_f32_e32 v20, v20
	v_lshlrev_b64 v[14:15], 10, v[14:15]
	v_lshl_add_u64 v[16:17], s[8:9], 0, v[0:1]
	v_lshl_add_u64 v[14:15], v[14:15], 0, v[2:3]
	global_store_dwordx4 v[16:17], v[6:9], off
	v_lshlrev_b64 v[14:15], 1, v[14:15]
	v_lshl_add_u64 v[18:19], s[6:7], 0, v[14:15]
	v_lshl_add_u64 v[14:15], s[8:9], 0, v[14:15]
	s_waitcnt vmcnt(1)
	v_lshlrev_b32_e32 v6, 16, v10
	v_and_b32_e32 v7, 0xffff0000, v10
	v_lshlrev_b32_e32 v8, 16, v11
	v_and_b32_e32 v9, 0xffff0000, v11
	v_lshlrev_b32_e32 v10, 16, v12
	v_and_b32_e32 v11, 0xffff0000, v12
	v_lshlrev_b32_e32 v12, 16, v13
	v_and_b32_e32 v13, 0xffff0000, v13
	v_mul_f32_e32 v5, v5, v6
	v_mul_f32_e32 v6, v21, v7
	v_mul_f32_e32 v7, v22, v8
	v_mul_f32_e32 v8, v23, v9
	v_mul_f32_e32 v9, v24, v10
	v_mul_f32_e32 v10, v25, v11
	v_mul_f32_e32 v11, v26, v12
	v_mul_f32_e32 v12, v20, v13
	v_cvt_pk_bf16_f32 v6, v5, v6
	v_cvt_pk_bf16_f32 v7, v7, v8
	v_cvt_pk_bf16_f32 v8, v9, v10
	v_cvt_pk_bf16_f32 v9, v11, v12
	global_store_dwordx4 v[16:17], v[6:9], off offset:256
	global_load_dwordx4 v[6:9], v[18:19], off nt
	v_mul_f32_e32 v10, 0xbfb8aa3b, v143
	v_mul_f32_e32 v11, 0xbfb8aa3b, v144
	v_mul_f32_e32 v12, 0xbfb8aa3b, v145
	v_mul_f32_e32 v13, 0xbfb8aa3b, v138
	v_mul_f32_e32 v16, 0xbfb8aa3b, v139
	v_mul_f32_e32 v17, 0xbfb8aa3b, v140
	v_mul_f32_e32 v20, 0xbfb8aa3b, v141
	v_mul_f32_e32 v5, 0xbfb8aa3b, v142
	v_exp_f32_e32 v10, v10
	v_exp_f32_e32 v11, v11
	v_exp_f32_e32 v12, v12
	v_exp_f32_e32 v13, v13
	v_exp_f32_e32 v16, v16
	v_exp_f32_e32 v17, v17
	v_exp_f32_e32 v20, v20
	v_exp_f32_e32 v5, v5
	v_add_f32_e32 v10, 1.0, v10
	v_add_f32_e32 v11, 1.0, v11
	v_add_f32_e32 v12, 1.0, v12
	v_add_f32_e32 v13, 1.0, v13
	v_add_f32_e32 v16, 1.0, v16
	v_add_f32_e32 v17, 1.0, v17
	v_add_f32_e32 v20, 1.0, v20
	v_add_f32_e32 v5, 1.0, v5
	v_rcp_f32_e32 v10, v10
	v_rcp_f32_e32 v11, v11
	v_rcp_f32_e32 v12, v12
	v_rcp_f32_e32 v13, v13
	v_rcp_f32_e32 v16, v16
	v_rcp_f32_e32 v17, v17
	v_rcp_f32_e32 v20, v20
	v_rcp_f32_e32 v5, v5
	s_waitcnt vmcnt(0)
	v_lshlrev_b32_e32 v21, 16, v6
	v_and_b32_e32 v6, 0xffff0000, v6
	v_lshlrev_b32_e32 v22, 16, v7
	v_and_b32_e32 v7, 0xffff0000, v7
	v_lshlrev_b32_e32 v23, 16, v8
	v_and_b32_e32 v8, 0xffff0000, v8
	v_lshlrev_b32_e32 v24, 16, v9
	v_and_b32_e32 v9, 0xffff0000, v9
	v_mul_f32_e32 v6, v10, v6
	v_mul_f32_e32 v10, v11, v22
	v_mul_f32_e32 v7, v12, v7
	v_mul_f32_e32 v11, v13, v23
	v_mul_f32_e32 v8, v16, v8
	v_mul_f32_e32 v12, v17, v24
	v_mul_f32_e32 v9, v20, v9
	v_mul_f32_e32 v5, v5, v21
	v_cvt_pk_bf16_f32 v6, v5, v6
	v_cvt_pk_bf16_f32 v7, v10, v7
	v_cvt_pk_bf16_f32 v8, v11, v8
	v_cvt_pk_bf16_f32 v9, v12, v9
	global_load_dwordx4 v[10:13], v[18:19], off offset:256 nt
	v_mul_f32_e32 v5, 0xbfb8aa3b, v134
	v_mul_f32_e32 v16, 0xbfb8aa3b, v135
	v_mul_f32_e32 v17, 0xbfb8aa3b, v136
	v_mul_f32_e32 v18, 0xbfb8aa3b, v137
	v_mul_f32_e32 v19, 0xbfb8aa3b, v130
	v_mul_f32_e32 v20, 0xbfb8aa3b, v131
	v_mul_f32_e32 v21, 0xbfb8aa3b, v132
	v_mul_f32_e32 v22, 0xbfb8aa3b, v133
	v_exp_f32_e32 v5, v5
	v_exp_f32_e32 v23, v16
	v_exp_f32_e32 v24, v17
	v_exp_f32_e32 v18, v18
	v_exp_f32_e32 v19, v19
	v_exp_f32_e32 v20, v20
	v_exp_f32_e32 v21, v21
	v_exp_f32_e32 v22, v22
	v_add_f32_e32 v5, 1.0, v5
	v_add_f32_e32 v23, 1.0, v23
	v_add_f32_e32 v24, 1.0, v24
	v_add_f32_e32 v18, 1.0, v18
	v_add_f32_e32 v19, 1.0, v19
	v_or_b32_e32 v16, 32, v4
	v_add_f32_e32 v20, 1.0, v20
	v_add_f32_e32 v21, 1.0, v21
	v_add_f32_e32 v22, 1.0, v22
	v_rcp_f32_e32 v5, v5
	v_rcp_f32_e32 v23, v23
	v_rcp_f32_e32 v24, v24
	v_rcp_f32_e32 v25, v18
	v_rcp_f32_e32 v26, v19
	v_ashrrev_i32_e32 v17, 31, v16
	v_rcp_f32_e32 v20, v20
	v_rcp_f32_e32 v21, v21
	v_rcp_f32_e32 v22, v22
	v_lshlrev_b64 v[16:17], 10, v[16:17]
	v_lshl_add_u64 v[16:17], v[16:17], 0, v[2:3]
	global_store_dwordx4 v[14:15], v[6:9], off
	v_lshlrev_b64 v[16:17], 1, v[16:17]
	v_lshl_add_u64 v[18:19], s[6:7], 0, v[16:17]
	v_or_b32_e32 v4, 48, v4
	v_lshl_add_u64 v[16:17], s[8:9], 0, v[16:17]
	s_waitcnt vmcnt(1)
	v_lshlrev_b32_e32 v6, 16, v10
	v_and_b32_e32 v7, 0xffff0000, v10
	v_lshlrev_b32_e32 v8, 16, v11
	v_and_b32_e32 v9, 0xffff0000, v11
	v_lshlrev_b32_e32 v10, 16, v12
	v_and_b32_e32 v11, 0xffff0000, v12
	v_lshlrev_b32_e32 v12, 16, v13
	v_and_b32_e32 v13, 0xffff0000, v13
	v_mul_f32_e32 v5, v5, v6
	v_mul_f32_e32 v6, v23, v7
	v_mul_f32_e32 v7, v24, v8
	v_mul_f32_e32 v8, v25, v9
	v_mul_f32_e32 v9, v26, v10
	v_mul_f32_e32 v10, v20, v11
	v_mul_f32_e32 v11, v21, v12
	v_mul_f32_e32 v12, v22, v13
	v_cvt_pk_bf16_f32 v6, v5, v6
	v_cvt_pk_bf16_f32 v7, v7, v8
	v_cvt_pk_bf16_f32 v8, v9, v10
	v_cvt_pk_bf16_f32 v9, v11, v12
	global_store_dwordx4 v[14:15], v[6:9], off offset:256
	global_load_dwordx4 v[6:9], v[18:19], off nt
	v_mul_f32_e32 v10, 0xbfb8aa3b, v127
	v_mul_f32_e32 v11, 0xbfb8aa3b, v128
	v_mul_f32_e32 v12, 0xbfb8aa3b, v129
	v_mul_f32_e32 v13, 0xbfb8aa3b, v122
	v_mul_f32_e32 v14, 0xbfb8aa3b, v123
	v_mul_f32_e32 v15, 0xbfb8aa3b, v124
	v_mul_f32_e32 v20, 0xbfb8aa3b, v125
	v_mul_f32_e32 v5, 0xbfb8aa3b, v126
	v_exp_f32_e32 v10, v10
	v_exp_f32_e32 v11, v11
	v_exp_f32_e32 v12, v12
	v_exp_f32_e32 v13, v13
	v_exp_f32_e32 v14, v14
	v_exp_f32_e32 v15, v15
	v_exp_f32_e32 v20, v20
	v_exp_f32_e32 v5, v5
	v_add_f32_e32 v10, 1.0, v10
	v_add_f32_e32 v11, 1.0, v11
	v_add_f32_e32 v12, 1.0, v12
	v_add_f32_e32 v13, 1.0, v13
	v_add_f32_e32 v14, 1.0, v14
	v_add_f32_e32 v15, 1.0, v15
	v_add_f32_e32 v20, 1.0, v20
	v_add_f32_e32 v5, 1.0, v5
	v_rcp_f32_e32 v10, v10
	v_rcp_f32_e32 v11, v11
	v_rcp_f32_e32 v12, v12
	v_rcp_f32_e32 v13, v13
	v_rcp_f32_e32 v14, v14
	v_rcp_f32_e32 v15, v15
	v_rcp_f32_e32 v20, v20
	v_rcp_f32_e32 v5, v5
	s_waitcnt vmcnt(0)
	v_lshlrev_b32_e32 v21, 16, v6
	v_and_b32_e32 v6, 0xffff0000, v6
	v_lshlrev_b32_e32 v22, 16, v7
	v_and_b32_e32 v7, 0xffff0000, v7
	v_lshlrev_b32_e32 v23, 16, v8
	v_and_b32_e32 v8, 0xffff0000, v8
	v_lshlrev_b32_e32 v24, 16, v9
	v_and_b32_e32 v9, 0xffff0000, v9
	v_mul_f32_e32 v6, v10, v6
	v_mul_f32_e32 v10, v11, v22
	v_mul_f32_e32 v7, v12, v7
	v_mul_f32_e32 v11, v13, v23
	v_mul_f32_e32 v8, v14, v8
	v_mul_f32_e32 v12, v15, v24
	v_mul_f32_e32 v9, v20, v9
	v_mul_f32_e32 v5, v5, v21
	v_cvt_pk_bf16_f32 v6, v5, v6
	v_cvt_pk_bf16_f32 v7, v10, v7
	v_cvt_pk_bf16_f32 v8, v11, v8
	v_cvt_pk_bf16_f32 v9, v12, v9
	global_load_dwordx4 v[10:13], v[18:19], off offset:256 nt
	v_mul_f32_e32 v5, 0xbfb8aa3b, v118
	v_mul_f32_e32 v14, 0xbfb8aa3b, v119
	v_mul_f32_e32 v15, 0xbfb8aa3b, v120
	v_mul_f32_e32 v18, 0xbfb8aa3b, v121
	v_mul_f32_e32 v19, 0xbfb8aa3b, v114
	v_mul_f32_e32 v20, 0xbfb8aa3b, v115
	v_mul_f32_e32 v21, 0xbfb8aa3b, v116
	v_mul_f32_e32 v22, 0xbfb8aa3b, v117
	v_exp_f32_e32 v23, v5
	v_exp_f32_e32 v14, v14
	v_exp_f32_e32 v15, v15
	v_exp_f32_e32 v18, v18
	v_exp_f32_e32 v19, v19
	v_exp_f32_e32 v20, v20
	v_exp_f32_e32 v21, v21
	v_exp_f32_e32 v22, v22
	v_add_f32_e32 v23, 1.0, v23
	v_add_f32_e32 v14, 1.0, v14
	v_add_f32_e32 v15, 1.0, v15
	v_add_f32_e32 v18, 1.0, v18
	v_ashrrev_i32_e32 v5, 31, v4
	v_add_f32_e32 v19, 1.0, v19
	v_add_f32_e32 v20, 1.0, v20
	v_add_f32_e32 v21, 1.0, v21
	v_add_f32_e32 v22, 1.0, v22
	v_rcp_f32_e32 v23, v23
	v_rcp_f32_e32 v24, v14
	v_rcp_f32_e32 v25, v15
	v_rcp_f32_e32 v26, v18
	v_lshlrev_b64 v[4:5], 10, v[4:5]
	v_rcp_f32_e32 v27, v19
	v_rcp_f32_e32 v20, v20
	v_rcp_f32_e32 v21, v21
	v_rcp_f32_e32 v22, v22
	v_lshl_add_u64 v[2:3], v[4:5], 0, v[2:3]
	v_lshlrev_b64 v[14:15], 1, v[2:3]
	global_store_dwordx4 v[16:17], v[6:9], off
	v_lshl_add_u64 v[18:19], s[6:7], 0, v[14:15]
	s_waitcnt vmcnt(1)
	v_lshlrev_b32_e32 v2, 16, v10
	v_and_b32_e32 v3, 0xffff0000, v10
	v_lshlrev_b32_e32 v4, 16, v11
	v_and_b32_e32 v5, 0xffff0000, v11
	v_lshlrev_b32_e32 v6, 16, v12
	v_and_b32_e32 v7, 0xffff0000, v12
	v_lshlrev_b32_e32 v8, 16, v13
	v_and_b32_e32 v9, 0xffff0000, v13
	v_mul_f32_e32 v2, v23, v2
	v_mul_f32_e32 v3, v24, v3
	v_mul_f32_e32 v4, v25, v4
	v_mul_f32_e32 v5, v26, v5
	v_mul_f32_e32 v6, v27, v6
	v_mul_f32_e32 v7, v20, v7
	v_mul_f32_e32 v8, v21, v8
	v_mul_f32_e32 v9, v22, v9
	v_cvt_pk_bf16_f32 v2, v2, v3
	v_cvt_pk_bf16_f32 v3, v4, v5
	v_cvt_pk_bf16_f32 v4, v6, v7
	v_cvt_pk_bf16_f32 v5, v8, v9
	global_store_dwordx4 v[16:17], v[2:5], off offset:256
	global_load_dwordx4 v[2:5], v[18:19], off nt
	v_mul_f32_e32 v6, 0xbfb8aa3b, v110
	v_mul_f32_e32 v7, 0xbfb8aa3b, v111
	v_mul_f32_e32 v8, 0xbfb8aa3b, v112
	v_mul_f32_e32 v9, 0xbfb8aa3b, v113
	v_mul_f32_e32 v10, 0xbfb8aa3b, v106
	v_mul_f32_e32 v11, 0xbfb8aa3b, v107
	v_mul_f32_e32 v12, 0xbfb8aa3b, v108
	v_mul_f32_e32 v13, 0xbfb8aa3b, v109
	v_exp_f32_e32 v6, v6
	v_exp_f32_e32 v7, v7
	v_exp_f32_e32 v8, v8
	v_exp_f32_e32 v9, v9
	v_exp_f32_e32 v10, v10
	v_exp_f32_e32 v11, v11
	v_exp_f32_e32 v12, v12
	v_exp_f32_e32 v13, v13
	v_add_f32_e32 v6, 1.0, v6
	v_add_f32_e32 v7, 1.0, v7
	v_add_f32_e32 v8, 1.0, v8
	v_add_f32_e32 v9, 1.0, v9
	v_add_f32_e32 v10, 1.0, v10
	v_add_f32_e32 v11, 1.0, v11
	v_add_f32_e32 v12, 1.0, v12
	v_add_f32_e32 v13, 1.0, v13
	v_rcp_f32_e32 v6, v6
	v_rcp_f32_e32 v7, v7
	v_rcp_f32_e32 v8, v8
	v_rcp_f32_e32 v9, v9
	v_rcp_f32_e32 v10, v10
	v_rcp_f32_e32 v11, v11
	v_rcp_f32_e32 v12, v12
	v_rcp_f32_e32 v13, v13
	s_waitcnt vmcnt(0)
	v_lshlrev_b32_e32 v16, 16, v2
	v_and_b32_e32 v2, 0xffff0000, v2
	v_lshlrev_b32_e32 v17, 16, v3
	v_and_b32_e32 v3, 0xffff0000, v3
	v_lshlrev_b32_e32 v20, 16, v4
	v_and_b32_e32 v4, 0xffff0000, v4
	v_lshlrev_b32_e32 v21, 16, v5
	v_and_b32_e32 v5, 0xffff0000, v5
	v_mul_f32_e32 v6, v6, v16
	v_mul_f32_e32 v2, v7, v2
	v_mul_f32_e32 v7, v8, v17
	v_mul_f32_e32 v3, v9, v3
	v_mul_f32_e32 v8, v10, v20
	v_mul_f32_e32 v4, v11, v4
	v_mul_f32_e32 v9, v12, v21
	v_mul_f32_e32 v5, v13, v5
	v_cvt_pk_bf16_f32 v2, v6, v2
	v_cvt_pk_bf16_f32 v3, v7, v3
	v_cvt_pk_bf16_f32 v4, v8, v4
	v_cvt_pk_bf16_f32 v5, v9, v5
	global_load_dwordx4 v[6:9], v[18:19], off offset:256 nt
	v_mul_f32_e32 v10, 0xbfb8aa3b, v102
	v_mul_f32_e32 v11, 0xbfb8aa3b, v103
	v_mul_f32_e32 v12, 0xbfb8aa3b, v104
	v_mul_f32_e32 v13, 0xbfb8aa3b, v105
	v_mul_f32_e32 v16, 0xbfb8aa3b, v98
	v_mul_f32_e32 v17, 0xbfb8aa3b, v99
	v_mul_f32_e32 v18, 0xbfb8aa3b, v100
	v_mul_f32_e32 v19, 0xbfb8aa3b, v101
	v_exp_f32_e32 v10, v10
	v_exp_f32_e32 v11, v11
	v_exp_f32_e32 v12, v12
	v_exp_f32_e32 v13, v13
	v_exp_f32_e32 v16, v16
	v_exp_f32_e32 v17, v17
	v_exp_f32_e32 v18, v18
	v_exp_f32_e32 v19, v19
	v_add_f32_e32 v10, 1.0, v10
	v_add_f32_e32 v11, 1.0, v11
	v_add_f32_e32 v12, 1.0, v12
	v_add_f32_e32 v13, 1.0, v13
	v_add_f32_e32 v16, 1.0, v16
	v_add_f32_e32 v17, 1.0, v17
	v_add_f32_e32 v18, 1.0, v18
	v_add_f32_e32 v19, 1.0, v19
	v_rcp_f32_e32 v20, v10
	v_rcp_f32_e32 v21, v11
	v_rcp_f32_e32 v22, v12
	v_rcp_f32_e32 v23, v13
	v_rcp_f32_e32 v16, v16
	v_rcp_f32_e32 v17, v17
	v_rcp_f32_e32 v18, v18
	v_rcp_f32_e32 v19, v19
	v_lshl_add_u64 v[12:13], s[8:9], 0, v[14:15]
	global_store_dwordx4 v[12:13], v[2:5], off
	v_lshl_add_u64 v[10:11], v[0:1], 0, s[20:21]
	v_lshl_add_u64 v[14:15], s[6:7], 0, v[10:11]
	v_lshl_add_u64 v[10:11], s[8:9], 0, v[10:11]
	s_mov_b64 s[20:21], 0x48000
	s_waitcnt vmcnt(1)
	v_lshlrev_b32_e32 v2, 16, v6
	v_and_b32_e32 v3, 0xffff0000, v6
	v_lshlrev_b32_e32 v4, 16, v7
	v_and_b32_e32 v5, 0xffff0000, v7
	v_lshlrev_b32_e32 v6, 16, v8
	v_and_b32_e32 v7, 0xffff0000, v8
	v_lshlrev_b32_e32 v8, 16, v9
	v_and_b32_e32 v9, 0xffff0000, v9
	v_mul_f32_e32 v2, v20, v2
	v_mul_f32_e32 v3, v21, v3
	v_mul_f32_e32 v4, v22, v4
	v_mul_f32_e32 v5, v23, v5
	v_mul_f32_e32 v6, v16, v6
	v_mul_f32_e32 v7, v17, v7
	v_mul_f32_e32 v8, v18, v8
	v_mul_f32_e32 v9, v19, v9
	v_cvt_pk_bf16_f32 v2, v2, v3
	v_cvt_pk_bf16_f32 v3, v4, v5
	v_cvt_pk_bf16_f32 v4, v6, v7
	v_cvt_pk_bf16_f32 v5, v8, v9
	global_store_dwordx4 v[12:13], v[2:5], off offset:256
	global_load_dwordx4 v[2:5], v[14:15], off nt
	v_mul_f32_e32 v6, 0xbfb8aa3b, v94
	v_mul_f32_e32 v7, 0xbfb8aa3b, v95
	v_mul_f32_e32 v8, 0xbfb8aa3b, v96
	v_mul_f32_e32 v9, 0xbfb8aa3b, v97
	v_mul_f32_e32 v12, 0xbfb8aa3b, v90
	v_mul_f32_e32 v13, 0xbfb8aa3b, v91
	v_mul_f32_e32 v16, 0xbfb8aa3b, v92
	v_mul_f32_e32 v17, 0xbfb8aa3b, v93
	v_exp_f32_e32 v6, v6
	v_exp_f32_e32 v7, v7
	v_exp_f32_e32 v8, v8
	v_exp_f32_e32 v9, v9
	v_exp_f32_e32 v12, v12
	v_exp_f32_e32 v13, v13
	v_exp_f32_e32 v16, v16
	v_exp_f32_e32 v17, v17
	v_add_f32_e32 v6, 1.0, v6
	v_add_f32_e32 v7, 1.0, v7
	v_add_f32_e32 v8, 1.0, v8
	v_add_f32_e32 v9, 1.0, v9
	v_add_f32_e32 v12, 1.0, v12
	v_add_f32_e32 v13, 1.0, v13
	v_add_f32_e32 v16, 1.0, v16
	v_add_f32_e32 v17, 1.0, v17
	v_rcp_f32_e32 v6, v6
	v_rcp_f32_e32 v7, v7
	v_rcp_f32_e32 v8, v8
	v_rcp_f32_e32 v9, v9
	v_rcp_f32_e32 v12, v12
	v_rcp_f32_e32 v13, v13
	v_rcp_f32_e32 v16, v16
	v_rcp_f32_e32 v17, v17
	s_waitcnt vmcnt(0)
	v_lshlrev_b32_e32 v18, 16, v2
	v_and_b32_e32 v2, 0xffff0000, v2
	v_lshlrev_b32_e32 v19, 16, v3
	v_and_b32_e32 v3, 0xffff0000, v3
	v_lshlrev_b32_e32 v20, 16, v4
	v_and_b32_e32 v4, 0xffff0000, v4
	v_lshlrev_b32_e32 v21, 16, v5
	v_and_b32_e32 v5, 0xffff0000, v5
	v_mul_f32_e32 v6, v6, v18
	v_mul_f32_e32 v2, v7, v2
	v_mul_f32_e32 v7, v8, v19
	v_mul_f32_e32 v3, v9, v3
	v_mul_f32_e32 v8, v12, v20
	v_mul_f32_e32 v4, v13, v4
	v_mul_f32_e32 v9, v16, v21
	v_mul_f32_e32 v5, v17, v5
	v_cvt_pk_bf16_f32 v2, v6, v2
	v_cvt_pk_bf16_f32 v3, v7, v3
	v_cvt_pk_bf16_f32 v4, v8, v4
	v_cvt_pk_bf16_f32 v5, v9, v5
	global_load_dwordx4 v[6:9], v[14:15], off offset:256 nt
	v_mul_f32_e32 v12, 0xbfb8aa3b, v86
	v_mul_f32_e32 v13, 0xbfb8aa3b, v87
	v_mul_f32_e32 v14, 0xbfb8aa3b, v88
	v_mul_f32_e32 v15, 0xbfb8aa3b, v89
	v_mul_f32_e32 v16, 0xbfb8aa3b, v82
	v_mul_f32_e32 v17, 0xbfb8aa3b, v83
	v_mul_f32_e32 v18, 0xbfb8aa3b, v84
	v_mul_f32_e32 v19, 0xbfb8aa3b, v85
	v_exp_f32_e32 v12, v12
	v_exp_f32_e32 v13, v13
	v_exp_f32_e32 v14, v14
	v_exp_f32_e32 v15, v15
	v_exp_f32_e32 v16, v16
	v_exp_f32_e32 v17, v17
	v_exp_f32_e32 v18, v18
	v_exp_f32_e32 v19, v19
	v_add_f32_e32 v12, 1.0, v12
	v_add_f32_e32 v13, 1.0, v13
	v_add_f32_e32 v14, 1.0, v14
	v_add_f32_e32 v15, 1.0, v15
	v_add_f32_e32 v16, 1.0, v16
	v_add_f32_e32 v17, 1.0, v17
	v_add_f32_e32 v18, 1.0, v18
	v_add_f32_e32 v19, 1.0, v19
	v_rcp_f32_e32 v20, v12
	v_rcp_f32_e32 v21, v13
	v_rcp_f32_e32 v22, v14
	v_rcp_f32_e32 v23, v15
	v_rcp_f32_e32 v16, v16
	v_rcp_f32_e32 v17, v17
	v_rcp_f32_e32 v18, v18
	v_rcp_f32_e32 v19, v19
	global_store_dwordx4 v[10:11], v[2:5], off
	v_lshl_add_u64 v[12:13], v[0:1], 0, s[20:21]
	v_lshl_add_u64 v[14:15], s[6:7], 0, v[12:13]
	v_lshl_add_u64 v[12:13], s[8:9], 0, v[12:13]
	s_mov_b64 s[20:21], 0x50000
	s_waitcnt vmcnt(1)
	v_lshlrev_b32_e32 v2, 16, v6
	v_and_b32_e32 v3, 0xffff0000, v6
	v_lshlrev_b32_e32 v4, 16, v7
	v_and_b32_e32 v5, 0xffff0000, v7
	v_lshlrev_b32_e32 v6, 16, v8
	v_and_b32_e32 v7, 0xffff0000, v8
	v_lshlrev_b32_e32 v8, 16, v9
	v_and_b32_e32 v9, 0xffff0000, v9
	v_mul_f32_e32 v2, v20, v2
	v_mul_f32_e32 v3, v21, v3
	v_mul_f32_e32 v4, v22, v4
	v_mul_f32_e32 v5, v23, v5
	v_mul_f32_e32 v6, v16, v6
	v_mul_f32_e32 v7, v17, v7
	v_mul_f32_e32 v8, v18, v8
	v_mul_f32_e32 v9, v19, v9
	v_cvt_pk_bf16_f32 v2, v2, v3
	v_cvt_pk_bf16_f32 v3, v4, v5
	v_cvt_pk_bf16_f32 v4, v6, v7
	v_cvt_pk_bf16_f32 v5, v8, v9
	global_store_dwordx4 v[10:11], v[2:5], off offset:256
	global_load_dwordx4 v[2:5], v[14:15], off nt
	v_mul_f32_e32 v6, 0xbfb8aa3b, v78
	v_mul_f32_e32 v7, 0xbfb8aa3b, v79
	v_mul_f32_e32 v8, 0xbfb8aa3b, v80
	v_mul_f32_e32 v9, 0xbfb8aa3b, v81
	v_mul_f32_e32 v10, 0xbfb8aa3b, v74
	v_mul_f32_e32 v11, 0xbfb8aa3b, v75
	v_mul_f32_e32 v16, 0xbfb8aa3b, v76
	v_mul_f32_e32 v17, 0xbfb8aa3b, v77
	v_exp_f32_e32 v6, v6
	v_exp_f32_e32 v7, v7
	v_exp_f32_e32 v8, v8
	v_exp_f32_e32 v9, v9
	v_exp_f32_e32 v10, v10
	v_exp_f32_e32 v11, v11
	v_exp_f32_e32 v16, v16
	v_exp_f32_e32 v17, v17
	v_add_f32_e32 v6, 1.0, v6
	v_add_f32_e32 v7, 1.0, v7
	v_add_f32_e32 v8, 1.0, v8
	v_add_f32_e32 v9, 1.0, v9
	v_add_f32_e32 v10, 1.0, v10
	v_add_f32_e32 v11, 1.0, v11
	v_add_f32_e32 v16, 1.0, v16
	v_add_f32_e32 v17, 1.0, v17
	v_rcp_f32_e32 v6, v6
	v_rcp_f32_e32 v7, v7
	v_rcp_f32_e32 v8, v8
	v_rcp_f32_e32 v9, v9
	v_rcp_f32_e32 v10, v10
	v_rcp_f32_e32 v11, v11
	v_rcp_f32_e32 v16, v16
	v_rcp_f32_e32 v17, v17
	s_waitcnt vmcnt(0)
	v_lshlrev_b32_e32 v18, 16, v2
	v_and_b32_e32 v2, 0xffff0000, v2
	v_lshlrev_b32_e32 v19, 16, v3
	v_and_b32_e32 v3, 0xffff0000, v3
	v_lshlrev_b32_e32 v20, 16, v4
	v_and_b32_e32 v4, 0xffff0000, v4
	v_lshlrev_b32_e32 v21, 16, v5
	v_and_b32_e32 v5, 0xffff0000, v5
	v_mul_f32_e32 v6, v6, v18
	v_mul_f32_e32 v2, v7, v2
	v_mul_f32_e32 v7, v8, v19
	v_mul_f32_e32 v3, v9, v3
	v_mul_f32_e32 v8, v10, v20
	v_mul_f32_e32 v4, v11, v4
	v_mul_f32_e32 v9, v16, v21
	v_mul_f32_e32 v5, v17, v5
	v_cvt_pk_bf16_f32 v2, v6, v2
	v_cvt_pk_bf16_f32 v3, v7, v3
	v_cvt_pk_bf16_f32 v4, v8, v4
	v_cvt_pk_bf16_f32 v5, v9, v5
	global_load_dwordx4 v[6:9], v[14:15], off offset:256 nt
	v_mul_f32_e32 v10, 0xbfb8aa3b, v70
	v_mul_f32_e32 v11, 0xbfb8aa3b, v71
	v_mul_f32_e32 v14, 0xbfb8aa3b, v72
	v_mul_f32_e32 v15, 0xbfb8aa3b, v73
	v_mul_f32_e32 v16, 0xbfb8aa3b, v66
	v_mul_f32_e32 v17, 0xbfb8aa3b, v67
	v_mul_f32_e32 v18, 0xbfb8aa3b, v68
	v_mul_f32_e32 v19, 0xbfb8aa3b, v69
	v_exp_f32_e32 v10, v10
	v_exp_f32_e32 v11, v11
	v_exp_f32_e32 v14, v14
	v_exp_f32_e32 v15, v15
	v_exp_f32_e32 v16, v16
	v_exp_f32_e32 v17, v17
	v_exp_f32_e32 v18, v18
	v_exp_f32_e32 v19, v19
	v_add_f32_e32 v10, 1.0, v10
	v_add_f32_e32 v11, 1.0, v11
	v_add_f32_e32 v14, 1.0, v14
	v_add_f32_e32 v15, 1.0, v15
	v_add_f32_e32 v16, 1.0, v16
	v_add_f32_e32 v17, 1.0, v17
	v_add_f32_e32 v18, 1.0, v18
	v_add_f32_e32 v19, 1.0, v19
	v_rcp_f32_e32 v20, v10
	v_rcp_f32_e32 v21, v11
	v_rcp_f32_e32 v22, v14
	v_rcp_f32_e32 v23, v15
	v_rcp_f32_e32 v16, v16
	v_rcp_f32_e32 v17, v17
	v_rcp_f32_e32 v18, v18
	v_rcp_f32_e32 v19, v19
	global_store_dwordx4 v[12:13], v[2:5], off
	v_lshl_add_u64 v[10:11], v[0:1], 0, s[20:21]
	v_lshl_add_u64 v[14:15], s[6:7], 0, v[10:11]
	s_mov_b64 s[20:21], 0x58000
	v_lshl_add_u64 v[10:11], s[8:9], 0, v[10:11]
	s_waitcnt vmcnt(1)
	v_lshlrev_b32_e32 v2, 16, v6
	v_and_b32_e32 v3, 0xffff0000, v6
	v_lshlrev_b32_e32 v4, 16, v7
	v_and_b32_e32 v5, 0xffff0000, v7
	v_lshlrev_b32_e32 v6, 16, v8
	v_and_b32_e32 v7, 0xffff0000, v8
	v_lshlrev_b32_e32 v8, 16, v9
	v_and_b32_e32 v9, 0xffff0000, v9
	v_mul_f32_e32 v2, v20, v2
	v_mul_f32_e32 v3, v21, v3
	v_mul_f32_e32 v4, v22, v4
	v_mul_f32_e32 v5, v23, v5
	v_mul_f32_e32 v6, v16, v6
	v_mul_f32_e32 v7, v17, v7
	v_mul_f32_e32 v8, v18, v8
	v_mul_f32_e32 v9, v19, v9
	v_cvt_pk_bf16_f32 v2, v2, v3
	v_cvt_pk_bf16_f32 v3, v4, v5
	v_cvt_pk_bf16_f32 v4, v6, v7
	v_cvt_pk_bf16_f32 v5, v8, v9
	global_store_dwordx4 v[12:13], v[2:5], off offset:256
	global_load_dwordx4 v[2:5], v[14:15], off nt
	v_mul_f32_e32 v6, 0xbfb8aa3b, v60
	v_mul_f32_e32 v7, 0xbfb8aa3b, v61
	v_mul_f32_e32 v8, 0xbfb8aa3b, v62
	v_mul_f32_e32 v9, 0xbfb8aa3b, v63
	v_mul_f32_e32 v12, 0xbfb8aa3b, v56
	v_mul_f32_e32 v13, 0xbfb8aa3b, v57
	v_mul_f32_e32 v16, 0xbfb8aa3b, v58
	v_mul_f32_e32 v17, 0xbfb8aa3b, v59
	v_exp_f32_e32 v6, v6
	v_exp_f32_e32 v7, v7
	v_exp_f32_e32 v8, v8
	v_exp_f32_e32 v9, v9
	v_exp_f32_e32 v12, v12
	v_exp_f32_e32 v13, v13
	v_exp_f32_e32 v16, v16
	v_exp_f32_e32 v17, v17
	v_add_f32_e32 v6, 1.0, v6
	v_add_f32_e32 v7, 1.0, v7
	v_add_f32_e32 v8, 1.0, v8
	v_add_f32_e32 v9, 1.0, v9
	v_add_f32_e32 v12, 1.0, v12
	v_add_f32_e32 v13, 1.0, v13
	v_add_f32_e32 v16, 1.0, v16
	v_add_f32_e32 v17, 1.0, v17
	v_rcp_f32_e32 v6, v6
	v_rcp_f32_e32 v7, v7
	v_rcp_f32_e32 v8, v8
	v_rcp_f32_e32 v9, v9
	v_rcp_f32_e32 v12, v12
	v_rcp_f32_e32 v13, v13
	v_rcp_f32_e32 v16, v16
	v_rcp_f32_e32 v17, v17
	s_waitcnt vmcnt(0)
	v_lshlrev_b32_e32 v18, 16, v2
	v_and_b32_e32 v2, 0xffff0000, v2
	v_lshlrev_b32_e32 v19, 16, v3
	v_and_b32_e32 v3, 0xffff0000, v3
	v_lshlrev_b32_e32 v20, 16, v4
	v_and_b32_e32 v4, 0xffff0000, v4
	v_lshlrev_b32_e32 v21, 16, v5
	v_and_b32_e32 v5, 0xffff0000, v5
	v_mul_f32_e32 v6, v6, v18
	v_mul_f32_e32 v2, v7, v2
	v_mul_f32_e32 v7, v8, v19
	v_mul_f32_e32 v3, v9, v3
	v_mul_f32_e32 v8, v12, v20
	v_mul_f32_e32 v4, v13, v4
	v_mul_f32_e32 v9, v16, v21
	v_mul_f32_e32 v5, v17, v5
	v_cvt_pk_bf16_f32 v2, v6, v2
	v_cvt_pk_bf16_f32 v3, v7, v3
	v_cvt_pk_bf16_f32 v4, v8, v4
	v_cvt_pk_bf16_f32 v5, v9, v5
	global_load_dwordx4 v[6:9], v[14:15], off offset:256 nt
	v_mul_f32_e32 v12, 0xbfb8aa3b, v52
	v_mul_f32_e32 v13, 0xbfb8aa3b, v53
	v_mul_f32_e32 v14, 0xbfb8aa3b, v54
	v_mul_f32_e32 v15, 0xbfb8aa3b, v55
	v_mul_f32_e32 v16, 0xbfb8aa3b, v48
	v_mul_f32_e32 v17, 0xbfb8aa3b, v49
	v_mul_f32_e32 v18, 0xbfb8aa3b, v50
	v_mul_f32_e32 v19, 0xbfb8aa3b, v51
	v_exp_f32_e32 v12, v12
	v_exp_f32_e32 v13, v13
	v_exp_f32_e32 v14, v14
	v_exp_f32_e32 v15, v15
	v_exp_f32_e32 v16, v16
	v_exp_f32_e32 v17, v17
	v_exp_f32_e32 v18, v18
	v_exp_f32_e32 v19, v19
	v_add_f32_e32 v12, 1.0, v12
	v_add_f32_e32 v13, 1.0, v13
	v_add_f32_e32 v14, 1.0, v14
	v_add_f32_e32 v15, 1.0, v15
	v_add_f32_e32 v16, 1.0, v16
	v_add_f32_e32 v17, 1.0, v17
	v_add_f32_e32 v18, 1.0, v18
	v_add_f32_e32 v19, 1.0, v19
	v_rcp_f32_e32 v20, v12
	v_rcp_f32_e32 v21, v13
	v_rcp_f32_e32 v22, v14
	v_rcp_f32_e32 v23, v15
	v_rcp_f32_e32 v16, v16
	v_rcp_f32_e32 v17, v17
	v_rcp_f32_e32 v18, v18
	v_rcp_f32_e32 v19, v19
	v_lshl_add_u64 v[12:13], v[0:1], 0, s[20:21]
	global_store_dwordx4 v[10:11], v[2:5], off
	v_lshl_add_u64 v[14:15], s[6:7], 0, v[12:13]
	s_mov_b64 s[20:21], -1
	s_waitcnt vmcnt(1)
	v_lshlrev_b32_e32 v0, 16, v6
	v_and_b32_e32 v1, 0xffff0000, v6
	v_lshlrev_b32_e32 v2, 16, v7
	v_and_b32_e32 v3, 0xffff0000, v7
	v_lshlrev_b32_e32 v4, 16, v8
	v_and_b32_e32 v5, 0xffff0000, v8
	v_lshlrev_b32_e32 v6, 16, v9
	v_and_b32_e32 v7, 0xffff0000, v9
	v_mul_f32_e32 v0, v20, v0
	v_mul_f32_e32 v1, v21, v1
	v_mul_f32_e32 v2, v22, v2
	v_mul_f32_e32 v3, v23, v3
	v_mul_f32_e32 v4, v16, v4
	v_mul_f32_e32 v5, v17, v5
	v_mul_f32_e32 v6, v18, v6
	v_mul_f32_e32 v7, v19, v7
	v_cvt_pk_bf16_f32 v0, v0, v1
	v_cvt_pk_bf16_f32 v1, v2, v3
	v_cvt_pk_bf16_f32 v2, v4, v5
	v_cvt_pk_bf16_f32 v3, v6, v7
	global_store_dwordx4 v[10:11], v[0:3], off offset:256
	global_load_dwordx4 v[0:3], v[14:15], off nt
	v_mul_f32_e32 v4, 0xbfb8aa3b, v44
	v_mul_f32_e32 v5, 0xbfb8aa3b, v45
	v_mul_f32_e32 v6, 0xbfb8aa3b, v46
	v_mul_f32_e32 v7, 0xbfb8aa3b, v47
	v_mul_f32_e32 v8, 0xbfb8aa3b, v40
	v_mul_f32_e32 v9, 0xbfb8aa3b, v41
	v_mul_f32_e32 v10, 0xbfb8aa3b, v42
	v_mul_f32_e32 v11, 0xbfb8aa3b, v43
	v_exp_f32_e32 v4, v4
	v_exp_f32_e32 v5, v5
	v_exp_f32_e32 v6, v6
	v_exp_f32_e32 v7, v7
	v_exp_f32_e32 v8, v8
	v_exp_f32_e32 v9, v9
	v_exp_f32_e32 v10, v10
	v_exp_f32_e32 v11, v11
	v_add_f32_e32 v4, 1.0, v4
	v_add_f32_e32 v5, 1.0, v5
	v_add_f32_e32 v6, 1.0, v6
	v_add_f32_e32 v7, 1.0, v7
	v_add_f32_e32 v8, 1.0, v8
	v_add_f32_e32 v9, 1.0, v9
	v_add_f32_e32 v10, 1.0, v10
	v_add_f32_e32 v11, 1.0, v11
	v_rcp_f32_e32 v4, v4
	v_rcp_f32_e32 v5, v5
	v_rcp_f32_e32 v6, v6
	v_rcp_f32_e32 v7, v7
	v_rcp_f32_e32 v8, v8
	v_rcp_f32_e32 v9, v9
	v_rcp_f32_e32 v10, v10
	v_rcp_f32_e32 v11, v11
	s_waitcnt vmcnt(0)
	v_lshlrev_b32_e32 v16, 16, v0
	v_and_b32_e32 v0, 0xffff0000, v0
	v_lshlrev_b32_e32 v17, 16, v1
	v_and_b32_e32 v1, 0xffff0000, v1
	v_lshlrev_b32_e32 v18, 16, v2
	v_and_b32_e32 v2, 0xffff0000, v2
	v_lshlrev_b32_e32 v19, 16, v3
	v_and_b32_e32 v3, 0xffff0000, v3
	v_mul_f32_e32 v4, v4, v16
	v_mul_f32_e32 v0, v5, v0
	v_mul_f32_e32 v5, v6, v17
	v_mul_f32_e32 v1, v7, v1
	v_mul_f32_e32 v6, v8, v18
	v_mul_f32_e32 v2, v9, v2
	v_mul_f32_e32 v7, v10, v19
	v_mul_f32_e32 v3, v11, v3
	v_cvt_pk_bf16_f32 v0, v4, v0
	v_cvt_pk_bf16_f32 v1, v5, v1
	v_cvt_pk_bf16_f32 v2, v6, v2
	v_cvt_pk_bf16_f32 v3, v7, v3
	global_load_dwordx4 v[4:7], v[14:15], off offset:256 nt
	v_mul_f32_e32 v8, 0xbfb8aa3b, v36
	v_mul_f32_e32 v9, 0xbfb8aa3b, v37
	v_mul_f32_e32 v10, 0xbfb8aa3b, v38
	v_mul_f32_e32 v11, 0xbfb8aa3b, v39
	v_mul_f32_e32 v14, 0xbfb8aa3b, v32
	v_mul_f32_e32 v15, 0xbfb8aa3b, v33
	v_mul_f32_e32 v16, 0xbfb8aa3b, v34
	v_mul_f32_e32 v17, 0xbfb8aa3b, v35
	v_exp_f32_e32 v8, v8
	v_exp_f32_e32 v9, v9
	v_exp_f32_e32 v10, v10
	v_exp_f32_e32 v11, v11
	v_exp_f32_e32 v14, v14
	v_exp_f32_e32 v15, v15
	v_exp_f32_e32 v16, v16
	v_exp_f32_e32 v17, v17
	v_add_f32_e32 v8, 1.0, v8
	v_add_f32_e32 v9, 1.0, v9
	v_add_f32_e32 v10, 1.0, v10
	v_add_f32_e32 v11, 1.0, v11
	v_add_f32_e32 v14, 1.0, v14
	v_add_f32_e32 v15, 1.0, v15
	v_add_f32_e32 v16, 1.0, v16
	v_add_f32_e32 v17, 1.0, v17
	v_rcp_f32_e32 v18, v8
	v_rcp_f32_e32 v19, v9
	v_rcp_f32_e32 v10, v10
	v_rcp_f32_e32 v11, v11
	v_rcp_f32_e32 v14, v14
	v_rcp_f32_e32 v15, v15
	v_rcp_f32_e32 v16, v16
	v_rcp_f32_e32 v17, v17
	v_lshl_add_u64 v[8:9], s[8:9], 0, v[12:13]
	global_store_dwordx4 v[8:9], v[0:3], off
	s_waitcnt vmcnt(1)
	s_nop 0
	v_lshlrev_b32_e32 v0, 16, v4
	v_and_b32_e32 v1, 0xffff0000, v4
	v_lshlrev_b32_e32 v2, 16, v5
	v_and_b32_e32 v3, 0xffff0000, v5
	v_lshlrev_b32_e32 v4, 16, v6
	v_and_b32_e32 v5, 0xffff0000, v6
	v_lshlrev_b32_e32 v6, 16, v7
	v_and_b32_e32 v7, 0xffff0000, v7
	v_mul_f32_e32 v0, v18, v0
	v_mul_f32_e32 v1, v19, v1
	v_mul_f32_e32 v2, v10, v2
	v_mul_f32_e32 v3, v11, v3
	v_mul_f32_e32 v4, v14, v4
	v_mul_f32_e32 v5, v15, v5
	v_mul_f32_e32 v6, v16, v6
	v_mul_f32_e32 v7, v17, v7
	v_cvt_pk_bf16_f32 v0, v0, v1
	v_cvt_pk_bf16_f32 v1, v2, v3
	v_cvt_pk_bf16_f32 v2, v4, v5
	v_cvt_pk_bf16_f32 v3, v6, v7
	global_store_dwordx4 v[8:9], v[0:3], off offset:256
	s_cbranch_vccnz .LBB0_2339
	s_andn2_b64 vcc, exec, s[4:5]
	s_cbranch_vccnz .LBB0_2338
	s_barrier
	s_branch .LBB0_2338
